# ROW_MIX layer0 row loop: header-top waits that only drained previous row stores removed, prefetched row waited at latch end
# baseline (speedup 1.0000x reference)
.LBB0_167:
	s_or_b64 exec, exec, s[0:1]
	v_readlane_b32 s0, v242, 1
	v_mov_b32_e32 v28, v208
	v_readlane_b32 s1, v242, 2
	s_waitcnt lgkmcnt(0)
	s_barrier
	s_nop 0
	s_mov_b32 s4, 0
	s_load_dword s2, s[0:1], 0x110
	s_add_u32 s0, s0, 0x110
	s_addc_u32 s1, s1, 0
	v_writelane_b32 v242, s0, 9
	v_ashrrev_i32_e32 v1, 6, v28
	s_waitcnt lgkmcnt(0)
	s_lshl_b32 s71, s2, 3
	s_abs_i32 s6, s71
	v_cvt_f32_u32_e32 v0, s6
	v_writelane_b32 v242, s1, 10
	s_mov_b32 s0, s2
	v_writelane_b32 v242, s0, 11
	v_rcp_iflag_f32_e32 v0, v0
	s_ashr_i32 s2, s71, 31
	v_writelane_b32 v242, s1, 12
	s_add_i32 s0, s71, 0x87ff
	v_mul_f32_e32 v0, 0x4f7ffffe, v0
	v_cvt_u32_f32_e32 v0, v0
	s_ashr_i32 s1, s0, 31
	v_writelane_b32 v242, s2, 13
	s_xor_b32 s1, s1, s2
	s_sub_i32 s2, 0, s6
	v_readfirstlane_b32 s3, v0
	s_mul_i32 s2, s2, s3
	s_mul_hi_u32 s2, s3, s2
	s_abs_i32 s0, s0
	s_add_i32 s2, s3, s2
	v_writelane_b32 v242, s2, 14
	s_mul_hi_u32 s2, s0, s2
	s_mul_i32 s3, s2, s6
	s_sub_i32 s0, s0, s3
	s_add_i32 s3, s2, 1
	s_sub_i32 s5, s0, s6
	s_cmp_ge_u32 s0, s6
	s_cselect_b32 s2, s3, s2
	s_cselect_b32 s0, s5, s0
	s_add_i32 s3, s2, 1
	s_cmp_ge_u32 s0, s6
	s_cselect_b32 s0, s3, s2
	v_writelane_b32 v242, s6, 15
	s_xor_b32 s0, s0, s1
	s_sub_i32 s1, s0, s1
	v_readlane_b32 s0, v242, 0
	s_lshl_b32 s0, s0, 3
	s_nop 0
	v_add_u32_e32 v0, s0, v1
	v_mul_lo_u32 v88, s1, v0
	v_add_u32_e32 v0, s1, v88
	v_min_i32_e32 v90, 0x8800, v0
	v_writelane_b32 v242, s0, 16
	v_cmp_lt_i32_e32 vcc, v88, v90
	v_writelane_b32 v242, s1, 17
	s_and_saveexec_b64 s[0:1], vcc
	s_cbranch_execz .LBB0_174
	v_readlane_b32 s10, v242, 1
	v_readlane_b32 s11, v242, 2
	s_load_dwordx2 s[2:3], s[10:11], s4 offset:0x0
	s_load_dwordx2 s[8:9], s[10:11], s4 offset:0x10
	s_load_dwordx2 s[6:7], s[10:11], s4 offset:0x30
	s_nop 0
	s_load_dwordx2 s[10:11], s[10:11], s4 offset:0x108
	s_mov_b32 s14, 0x8000
	v_add_u32_e32 v16, 0xffff8000, v88
	v_ashrrev_i32_e32 v89, 31, v88
	v_cmp_gt_i32_e32 vcc, s14, v88
	s_waitcnt lgkmcnt(0)
	v_mov_b32_e32 v18, s9
	v_mov_b32_e32 v19, s3
	v_lshlrev_b32_e32 v0, 2, v28
	v_cndmask_b32_e32 v17, 0, v89, vcc
	v_cndmask_b32_e32 v16, v16, v88, vcc
	v_cndmask_b32_e32 v19, v18, v19, vcc
	v_mov_b32_e32 v18, s8
	v_mov_b32_e32 v20, s2
	v_and_b32_e32 v30, 0xfc, v0
	v_cndmask_b32_e32 v18, v18, v20, vcc
	v_lshlrev_b64 v[16:17], 12, v[16:17]
	v_mov_b32_e32 v81, 0
	v_lshlrev_b32_e32 v80, 2, v30
	v_lshl_add_u64 v[16:17], v[18:19], 0, v[16:17]
	v_lshl_add_u64 v[32:33], v[16:17], 0, v[80:81]
	global_load_dwordx4 v[0:3], v80, s[6:7]
	global_load_dwordx4 v[4:7], v80, s[6:7] offset:1024
	global_load_dwordx4 v[8:11], v80, s[6:7] offset:2048
	global_load_dwordx4 v[12:15], v80, s[6:7] offset:3072
	global_load_dwordx4 v[36:39], v[32:33], off
	global_load_dwordx4 v[24:27], v[32:33], off offset:1024
	global_load_dwordx4 v[20:23], v[32:33], off offset:2048
	global_load_dwordx4 v[16:19], v[32:33], off offset:3072
	v_lshl_add_u64 v[32:33], s[10:11], 0, v[80:81]
	s_mov_b64 s[4:5], 0x4000
	v_lshl_add_u64 v[82:83], v[32:33], 0, s[4:5]
	v_lshlrev_b64 v[32:33], 11, v[88:89]
	v_and_b32_e32 v28, 63, v28
	v_lshl_or_b32 v32, v28, 3, v32
	v_lshl_add_u64 v[28:29], s[10:11], 0, v[32:33]
	s_mov_b64 s[4:5], 0xdbff000
	v_lshl_add_u64 v[84:85], v[28:29], 0, s[4:5]
	v_mov_b32_e32 v93, -1
	s_mov_b64 s[10:11], 0
	s_movk_i32 s15, 0x7fff
	v_lshlrev_b32_e32 v80, 2, v30
	v_mov_b32_e32 v91, 0x358637bd
	s_mov_b32 s16, 0xf800000
	v_mov_b32_e32 v92, 0x260
	s_mov_b64 s[12:13], 0x800
	s_waitcnt vmcnt(0)
	s_branch .LBB0_170
.LBB0_169:
	s_or_b64 exec, exec, s[6:7]
	v_mul_f32_e32 v88, v37, v37
	v_mul_f32_e32 v89, v25, v25
	v_fmac_f32_e32 v88, v36, v36
	v_fmac_f32_e32 v89, v24, v24
	v_fmac_f32_e32 v88, v38, v38
	v_fmac_f32_e32 v89, v26, v26
	v_fmac_f32_e32 v88, v39, v39
	v_fmac_f32_e32 v89, v27, v27
	v_add_f32_e32 v88, v89, v88
	v_mul_f32_e32 v89, v21, v21
	v_fmac_f32_e32 v89, v20, v20
	v_fmac_f32_e32 v89, v22, v22
	v_fmac_f32_e32 v89, v23, v23
	v_add_f32_e32 v88, v89, v88
	v_mul_f32_e32 v89, v17, v17
	v_fmac_f32_e32 v89, v16, v16
	v_fmac_f32_e32 v89, v18, v18
	v_fmac_f32_e32 v89, v19, v19
	v_add_f32_e32 v88, v89, v88
	s_and_b64 s[4:5], exec, s[4:5]
	s_or_b64 s[10:11], s[4:5], s[10:11]
	v_add_f32_dpp v88, v88, v88 quad_perm:[1,0,3,2] row_mask:0xf bank_mask:0xf bound_ctrl:1
	s_nop 1
	v_add_f32_dpp v88, v88, v88 quad_perm:[2,3,0,1] row_mask:0xf bank_mask:0xf bound_ctrl:1
	s_nop 1
	v_add_f32_dpp v88, v88, v88 row_half_mirror row_mask:0xf bank_mask:0xf bound_ctrl:1
	s_nop 1
	v_add_f32_dpp v88, v88, v88 row_mirror row_mask:0xf bank_mask:0xf bound_ctrl:1
	s_nop 0
	v_readlane_b32 s7, v88, 16
	v_readlane_b32 s6, v88, 0
	s_nop 0
	v_mov_b32_e32 v89, s7
	v_add_f32_e32 v89, s6, v89
	v_readlane_b32 s6, v88, 32
	s_nop 1
	v_add_f32_e32 v89, s6, v89
	v_readlane_b32 s6, v88, 48
	s_nop 1
	v_add_f32_e32 v88, s6, v89
	v_fmamk_f32 v88, v88, 0x3a800000, v91
	v_mul_f32_e32 v89, 0x4f800000, v88
	v_cmp_gt_f32_e32 vcc, s16, v88
	s_nop 1
	v_cndmask_b32_e32 v88, v88, v89, vcc
	v_sqrt_f32_e32 v89, v88
	s_nop 0
	v_add_u32_e32 v94, -1, v89
	v_fma_f32 v95, -v94, v89, v88
	v_cmp_ge_f32_e64 s[6:7], 0, v95
	v_add_u32_e32 v95, 1, v89
	s_nop 0
	v_cndmask_b32_e64 v94, v89, v94, s[6:7]
	v_fma_f32 v89, -v95, v89, v88
	v_cmp_lt_f32_e64 s[6:7], 0, v89
	s_nop 1
	v_cndmask_b32_e64 v89, v94, v95, s[6:7]
	v_mul_f32_e32 v94, 0x37800000, v89
	v_cndmask_b32_e32 v89, v89, v94, vcc
	v_cmp_class_f32_e32 vcc, v88, v92
	s_nop 1
	v_cndmask_b32_e32 v88, v89, v88, vcc
	v_div_scale_f32 v89, s[6:7], v88, v88, 1.0
	v_rcp_f32_e32 v94, v89
	s_nop 0
	v_fma_f32 v95, -v89, v94, 1.0
	v_fmac_f32_e32 v94, v95, v94
	v_div_scale_f32 v95, vcc, 1.0, v88, 1.0
	v_mul_f32_e32 v96, v95, v94
	v_fma_f32 v97, -v89, v96, v95
	v_fmac_f32_e32 v96, v97, v94
	v_fma_f32 v89, -v89, v96, v95
	v_div_fmas_f32 v89, v89, v94, v96
	v_div_fixup_f32 v88, v89, v88, 1.0
	v_pk_mul_f32 v[38:39], v[88:89], v[38:39] op_sel_hi:[0,1]
	v_pk_mul_f32 v[36:37], v[88:89], v[36:37] op_sel_hi:[0,1]
	v_pk_mul_f32 v[26:27], v[88:89], v[26:27] op_sel_hi:[0,1]
	v_pk_mul_f32 v[24:25], v[88:89], v[24:25] op_sel_hi:[0,1]
	v_pk_mul_f32 v[22:23], v[88:89], v[22:23] op_sel_hi:[0,1]
	v_pk_mul_f32 v[20:21], v[88:89], v[20:21] op_sel_hi:[0,1]
	v_pk_mul_f32 v[18:19], v[88:89], v[18:19] op_sel_hi:[0,1]
	v_pk_mul_f32 v[16:17], v[88:89], v[16:17] op_sel_hi:[0,1]
	v_pk_mul_f32 v[36:37], v[0:1], v[36:37]
	v_pk_mul_f32 v[38:39], v[2:3], v[38:39]
	v_pk_mul_f32 v[24:25], v[4:5], v[24:25]
	v_pk_mul_f32 v[26:27], v[6:7], v[26:27]
	v_pk_mul_f32 v[20:21], v[8:9], v[20:21]
	v_pk_mul_f32 v[22:23], v[10:11], v[22:23]
	v_pk_mul_f32 v[16:17], v[12:13], v[16:17]
	v_pk_mul_f32 v[18:19], v[14:15], v[18:19]
	v_pk_fma_f32 v[38:39], v[50:51], v[38:39], v[30:31]
	v_pk_fma_f32 v[36:37], v[48:49], v[36:37], v[28:29]
	v_pk_fma_f32 v[26:27], v[54:55], v[26:27], v[34:35]
	v_pk_fma_f32 v[24:25], v[52:53], v[24:25], v[32:33]
	v_pk_fma_f32 v[22:23], v[58:59], v[22:23], v[42:43]
	v_pk_fma_f32 v[20:21], v[56:57], v[20:21], v[40:41]
	v_pk_fma_f32 v[18:19], v[62:63], v[18:19], v[46:47]
	v_pk_fma_f32 v[16:17], v[60:61], v[16:17], v[44:45]
	v_cvt_pk_bf16_f32 v36, v36, v37
	v_cvt_pk_bf16_f32 v37, v38, v39
	v_cvt_pk_bf16_f32 v24, v24, v25
	v_cvt_pk_bf16_f32 v25, v26, v27
	v_cvt_pk_bf16_f32 v20, v20, v21
	v_cvt_pk_bf16_f32 v21, v22, v23
	v_cvt_pk_bf16_f32 v16, v16, v17
	v_cvt_pk_bf16_f32 v17, v18, v19
	global_store_dwordx2 v[84:85], v[36:37], off
	global_store_dwordx2 v[84:85], v[24:25], off offset:512
	global_store_dwordx2 v[84:85], v[20:21], off offset:1024
	global_store_dwordx2 v[84:85], v[16:17], off offset:1536
	s_waitcnt vmcnt(4)
	v_lshl_add_u64 v[84:85], v[84:85], 0, s[12:13]
	v_mov_b64_e32 v[88:89], v[86:87]
	v_mov_b32_e32 v36, v64
	v_mov_b32_e32 v37, v65
	v_mov_b32_e32 v38, v66
	v_mov_b32_e32 v39, v67
	v_mov_b32_e32 v24, v68
	v_mov_b32_e32 v25, v69
	v_mov_b32_e32 v26, v70
	v_mov_b32_e32 v27, v71
	v_mov_b32_e32 v20, v72
	v_mov_b32_e32 v21, v73
	v_mov_b32_e32 v22, v74
	v_mov_b32_e32 v23, v75
	v_mov_b32_e32 v16, v76
	v_mov_b32_e32 v17, v77
	v_mov_b32_e32 v18, v78
	v_mov_b32_e32 v19, v79
	s_andn2_b64 exec, exec, s[10:11]
	s_cbranch_execz .LBB0_174
.LBB0_170:
	v_lshl_add_u64 v[86:87], v[88:89], 0, 1
	v_cmp_lt_i32_e32 vcc, v86, v90
	v_cmp_ge_i32_e64 s[4:5], v86, v90
	v_mov_b32_e32 v64, v36
	v_mov_b32_e32 v65, v37
	v_mov_b32_e32 v66, v38
	v_mov_b32_e32 v67, v39
	v_mov_b32_e32 v68, v24
	v_mov_b32_e32 v69, v25
	v_mov_b32_e32 v70, v26
	v_mov_b32_e32 v71, v27
	v_mov_b32_e32 v72, v20
	v_mov_b32_e32 v73, v21
	v_mov_b32_e32 v74, v22
	v_mov_b32_e32 v75, v23
	v_mov_b32_e32 v76, v16
	v_mov_b32_e32 v77, v17
	v_mov_b32_e32 v78, v18
	v_mov_b32_e32 v79, v19
	s_and_saveexec_b64 s[6:7], vcc
	s_cbranch_execz .LBB0_172
	v_add_u32_e32 v64, 0xffff8001, v88
	v_cmp_gt_i32_e32 vcc, s15, v88
	v_mov_b32_e32 v66, s9
	v_mov_b32_e32 v67, s3
	v_cndmask_b32_e32 v65, 0, v87, vcc
	v_cndmask_b32_e32 v64, v64, v86, vcc
	v_cndmask_b32_e32 v67, v66, v67, vcc
	v_mov_b32_e32 v66, s8
	v_mov_b32_e32 v68, s2
	v_cndmask_b32_e32 v66, v66, v68, vcc
	v_lshlrev_b64 v[64:65], 12, v[64:65]
	v_lshl_add_u64 v[64:65], v[66:67], 0, v[64:65]
	v_lshl_add_u64 v[94:95], v[64:65], 0, v[80:81]
	global_load_dwordx4 v[64:67], v[94:95], off
	global_load_dwordx4 v[68:71], v[94:95], off offset:1024
	global_load_dwordx4 v[72:75], v[94:95], off offset:2048
	global_load_dwordx4 v[76:79], v[94:95], off offset:3072
.LBB0_172:
	s_or_b64 exec, exec, s[6:7]
	v_ashrrev_i32_e32 v89, 31, v88
	v_lshrrev_b32_e32 v89, 20, v89
	v_add_u32_e32 v89, v88, v89
	v_ashrrev_i32_e32 v89, 12, v89
	v_cmp_gt_i32_e32 vcc, s14, v88
	s_nop 1
	v_cndmask_b32_e32 v88, 8, v89, vcc
	v_cmp_ne_u32_e32 vcc, v88, v93
	s_and_saveexec_b64 s[6:7], vcc
	s_cbranch_execz .LBB0_169
	v_mul_hi_i32_i24_e32 v29, 0x6000, v88
	v_mul_i32_i24_e32 v28, 0x6000, v88
	v_lshl_add_u64 v[94:95], v[82:83], 0, v[28:29]
	v_add_co_u32_e32 v96, vcc, 0x1000, v94
	v_mov_b32_e32 v93, v88
	s_nop 0
	v_addc_co_u32_e32 v97, vcc, 0, v95, vcc
	global_load_dwordx4 v[48:51], v[96:97], off
	global_load_dwordx4 v[52:55], v[96:97], off offset:1024
	global_load_dwordx4 v[56:59], v[96:97], off offset:2048
	global_load_dwordx4 v[60:63], v[96:97], off offset:3072
	global_load_dwordx4 v[28:31], v[94:95], off
	global_load_dwordx4 v[32:35], v[94:95], off offset:1024
	global_load_dwordx4 v[40:43], v[94:95], off offset:2048
	global_load_dwordx4 v[44:47], v[94:95], off offset:3072
	s_waitcnt vmcnt(7)
	v_pk_add_f32 v[50:51], v[50:51], 1.0 op_sel_hi:[1,0]
	v_pk_add_f32 v[48:49], v[48:49], 1.0 op_sel_hi:[1,0]
	s_waitcnt vmcnt(6)
	v_pk_add_f32 v[54:55], v[54:55], 1.0 op_sel_hi:[1,0]
	v_pk_add_f32 v[52:53], v[52:53], 1.0 op_sel_hi:[1,0]
	s_waitcnt vmcnt(5)
	v_pk_add_f32 v[58:59], v[58:59], 1.0 op_sel_hi:[1,0]
	v_pk_add_f32 v[56:57], v[56:57], 1.0 op_sel_hi:[1,0]
	s_waitcnt vmcnt(4)
	v_pk_add_f32 v[62:63], v[62:63], 1.0 op_sel_hi:[1,0]
	v_pk_add_f32 v[60:61], v[60:61], 1.0 op_sel_hi:[1,0]
	s_waitcnt vmcnt(0)
	s_branch .LBB0_169
